# attention main loop: bias init (qf-fk) via v_mfma_f32_32x32x2_f32 instead of 32 v_sub + 8 ds_read_b128 per tile
# speedup vs baseline: 1.0016x; 1.0016x over previous
.LBB0_1700:
	s_cmp_lg_u32 0, -1
	s_waitcnt vmcnt(0) lgkmcnt(0)
	s_barrier
	s_cselect_b32 s9, 0, 0
	s_nop 8
	v_exp_f32_e32 v50, v2
	v_exp_f32_e32 v51, v3
	v_lshl_add_u64 v[2:3], v[214:215], 0, s[16:17]
	s_mov_b32 s8, m0
	s_mov_b32 m0, s50
	s_nop 0
	global_load_lds_dwordx4 v[2:3], off
	s_mov_b32 m0, s8
	s_add_i32 s9, s9, s30
	v_lshl_add_u64 v[216:217], v[34:35], 0, s[12:13]
	s_add_i32 s9, s9, 0x8000
	s_mov_b32 s30, m0
	s_mov_b32 m0, s9
	s_nop 0
	global_load_lds_dwordx4 v[216:217], off
	s_mov_b32 m0, s30
	ds_read_b128 v[174:177], v232 offset:8192
	ds_read_b128 v[166:169], v232 offset:8704
	ds_read_b128 v[170:173], v232 offset:10240
	ds_read_b128 v[158:161], v232 offset:10752
	ds_read_b128 v[162:165], v232 offset:12288
	ds_read_b128 v[150:153], v232 offset:12800
	ds_read_b128 v[154:157], v232 offset:14336
	ds_read_b128 v[146:149], v232 offset:14848
	v_exp_f32_e32 v66, v18
	v_exp_f32_e32 v67, v19
	v_exp_f32_e32 v68, v20
	v_exp_f32_e32 v69, v21
	v_exp_f32_e32 v70, v22
	v_exp_f32_e32 v71, v23
	v_exp_f32_e32 v72, v24
	v_exp_f32_e32 v73, v25
	v_exp_f32_e32 v74, v26
	v_exp_f32_e32 v75, v27
	v_exp_f32_e32 v76, v28
	v_exp_f32_e32 v77, v29
	v_exp_f32_e32 v78, v30
	v_exp_f32_e32 v79, v31
	v_exp_f32_e32 v80, v32
	v_exp_f32_e32 v81, v33
	v_exp_f32_e32 v52, v4
	v_exp_f32_e32 v53, v5
	v_exp_f32_e32 v54, v6
	v_exp_f32_e32 v55, v7
	v_exp_f32_e32 v56, v8
	v_exp_f32_e32 v57, v9
	v_exp_f32_e32 v58, v10
	v_exp_f32_e32 v59, v11
	v_exp_f32_e32 v60, v12
	v_exp_f32_e32 v61, v13
	v_exp_f32_e32 v62, v14
	v_exp_f32_e32 v63, v15
	v_exp_f32_e32 v64, v16
	v_exp_f32_e32 v65, v17
	s_waitcnt vmcnt(2) lgkmcnt(0)
	s_barrier
	s_mov_b32 s8, 0
	s_cmp_lt_i32 s49, 7
	s_mov_b32 s42, 0
	s_cbranch_scc1 .LBB0_1741
	v_lshl_add_u64 v[218:219], v[34:35], 0, s[16:17]
	v_mov_b32_e32 v34, 0
	s_add_i32 s9, s49, -5
	v_lshl_add_u64 v[220:221], v[214:215], 0, s[18:19]
	s_mov_b32 s30, 1
	s_movk_i32 s53, 0x4000
	s_movk_i32 s52, 0x2000
	v_mov_b32_e32 v35, v241
	v_and_b32_e32 v36, 63, v0
	v_lshlrev_b32_e32 v36, 2, v36
	v_and_b32_e32 v37, 32, v0
	v_lshrrev_b32_e32 v37, 1, v37
	v_sub_u32_e32 v36, v36, v37
	v_add_u32_e32 v245, v241, v36
	v_mov_b32_e32 v242, 1.0
	v_mov_b32_e32 v243, 1.0
	v_mov_b32_e32 v246, 1.0
	v_mov_b32_e32 v247, 1.0
	v_mov_b32_e32 v244, v213
	s_mov_b32 exec_hi, 0
	v_mov_b32_e32 v244, -1.0
	ds_read_b32 v242, v245
	ds_read_b32 v243, v245 offset:128
	s_mov_b32 exec_hi, -1
	s_waitcnt lgkmcnt(0)
	v_mov_b32_e32 v2, 0
	v_mov_b32_e32 v3, v34
	v_mov_b32_e32 v4, v34
	v_mov_b32_e32 v5, v34
	v_mov_b32_e32 v6, v34
	v_mov_b32_e32 v7, v34
	v_mov_b32_e32 v8, v34
	v_mov_b32_e32 v9, v34
	v_mov_b32_e32 v10, v34
	v_mov_b32_e32 v11, v34
	v_mov_b32_e32 v12, v34
	v_mov_b32_e32 v13, v34
	v_mov_b32_e32 v14, v34
	v_mov_b32_e32 v15, v34
	v_mov_b32_e32 v16, v34
	v_mov_b32_e32 v17, v34
	v_mov_b32_e32 v18, 0
	v_mov_b32_e32 v19, v34
	v_mov_b32_e32 v20, v34
	v_mov_b32_e32 v21, v34
	v_mov_b32_e32 v22, v34
	v_mov_b32_e32 v23, v34
	v_mov_b32_e32 v24, v34
	v_mov_b32_e32 v25, v34
	v_mov_b32_e32 v26, v34
	v_mov_b32_e32 v27, v34
	v_mov_b32_e32 v28, v34
	v_mov_b32_e32 v29, v34
	v_mov_b32_e32 v30, v34
	v_mov_b32_e32 v31, v34
	v_mov_b32_e32 v32, v34
	v_mov_b32_e32 v33, v34
.LBB0_1702:
	s_mov_b32 s8, s53
	s_mov_b32 s41, s52
	v_mfma_f32_32x32x2_f32 v[98:113], v242, v244, 0
	v_mfma_f32_32x32x2_f32 v[82:97], v243, v244, 0
	s_mov_b32 exec_hi, 0
	ds_read_b32 v246, v245 offset:256
	ds_read_b32 v247, v245 offset:384
	s_mov_b32 exec_hi, -1
	v_add_u32_e32 v178, s42, v235
	ds_read_b64_tr_b16 v[36:37], v178 offset:24576
	ds_read_b64_tr_b16 v[38:39], v178 offset:25088
	v_add_f32_e32 v40, v66, v67
	v_add_f32_e32 v40, v68, v40
	v_add_f32_e32 v40, v69, v40
	v_add_f32_e32 v40, v70, v40
	v_add_f32_e32 v44, v71, v40
	v_cvt_pk_bf16_f32 v130, v66, v67
	v_cvt_pk_bf16_f32 v131, v68, v69
	v_mfma_f32_32x32x16_bf16 v[98:113], v[174:177], v[114:117], v[98:113]
	ds_read_b64_tr_b16 v[40:41], v178 offset:28672
	ds_read_b64_tr_b16 v[42:43], v178 offset:29184
	v_add_f32_e32 v44, v72, v44
	v_add_f32_e32 v44, v73, v44
	v_add_f32_e32 v44, v74, v44
	v_add_f32_e32 v48, v75, v44
	v_cvt_pk_bf16_f32 v132, v70, v71
	v_cvt_pk_bf16_f32 v133, v72, v73
	v_mfma_f32_32x32x16_bf16 v[82:97], v[166:169], v[114:117], v[82:97]
	ds_read_b64_tr_b16 v[44:45], v178 offset:25600
	ds_read_b64_tr_b16 v[46:47], v178 offset:26112
	v_add_f32_e32 v48, v76, v48
	v_add_f32_e32 v48, v77, v48
	v_add_f32_e32 v48, v78, v48
	v_add_f32_e32 v48, v79, v48
	v_cvt_pk_bf16_f32 v134, v74, v75
	v_cvt_pk_bf16_f32 v135, v76, v77
	v_mfma_f32_32x32x16_bf16 v[98:113], v[170:173], v[118:121], v[98:113]
	ds_read_b64_tr_b16 v[66:67], v178 offset:29696
	ds_read_b64_tr_b16 v[68:69], v178 offset:30208
	v_add_f32_e32 v48, v80, v48
	v_add_f32_e32 v48, v81, v48
	v_add_f32_e32 v48, v50, v48
	v_add_f32_e32 v48, v51, v48
	v_cvt_pk_bf16_f32 v136, v78, v79
	v_cvt_pk_bf16_f32 v137, v80, v81
	v_mfma_f32_32x32x16_bf16 v[82:97], v[158:161], v[118:121], v[82:97]
	ds_read_b64_tr_b16 v[158:159], v178 offset:26624
	ds_read_b64_tr_b16 v[160:161], v178 offset:27136
	v_add_f32_e32 v48, v52, v48
	v_add_f32_e32 v48, v53, v48
	v_add_f32_e32 v48, v54, v48
	v_add_f32_e32 v70, v55, v48
	v_cvt_pk_bf16_f32 v138, v50, v51
	v_cvt_pk_bf16_f32 v139, v52, v53
	v_mfma_f32_32x32x16_bf16 v[98:113], v[162:165], v[122:125], v[98:113]
	ds_read_b64_tr_b16 v[48:49], v178 offset:30720
	ds_read_b64_tr_b16 v[50:51], v178 offset:31232
	v_add_f32_e32 v52, v56, v70
	v_add_f32_e32 v52, v57, v52
	v_add_f32_e32 v52, v58, v52
	v_add_f32_e32 v52, v59, v52
	v_cvt_pk_bf16_f32 v140, v54, v55
	v_cvt_pk_bf16_f32 v141, v56, v57
	v_mfma_f32_32x32x16_bf16 v[82:97], v[150:153], v[122:125], v[82:97]
	ds_read_b64_tr_b16 v[150:151], v178 offset:27648
	ds_read_b64_tr_b16 v[152:153], v178 offset:28160
	v_add_f32_e32 v52, v60, v52
	v_add_f32_e32 v52, v61, v52
	v_add_f32_e32 v52, v62, v52
	v_add_f32_e32 v52, v63, v52
	v_cvt_pk_bf16_f32 v142, v58, v59
	v_cvt_pk_bf16_f32 v143, v60, v61
	v_mfma_f32_32x32x16_bf16 v[98:113], v[154:157], v[126:129], v[98:113]
	ds_read_b64_tr_b16 v[166:167], v178 offset:31744
	ds_read_b64_tr_b16 v[168:169], v178 offset:32256
	v_add_f32_e32 v52, v64, v52
	v_add_f32_e32 v52, v65, v52
	v_add_f32_e32 v251, 0, v52
	v_cvt_pk_bf16_f32 v144, v62, v63
	v_cvt_pk_bf16_f32 v145, v64, v65
	v_mfma_f32_32x32x16_bf16 v[82:97], v[146:149], v[126:129], v[82:97]
	v_lshl_add_u64 v[52:53], v[220:221], 0, s[20:21]
	s_add_i32 s42, s52, s50
	s_mov_b32 s43, m0
	s_mov_b32 m0, s42
	s_nop 0
	global_load_lds_dwordx4 v[52:53], off
	s_mov_b32 m0, s43
	v_lshl_add_u64 v[52:53], v[218:219], 0, s[20:21]
	s_add_i32 s42, s53, s51
	s_mov_b32 s43, m0
	s_mov_b32 m0, s42
	s_nop 0
	global_load_lds_dwordx4 v[52:53], off
	s_mov_b32 m0, s43
	v_exp_f32_e32 v98, v98
	v_exp_f32_e32 v99, v99
	v_exp_f32_e32 v100, v100
	v_exp_f32_e32 v101, v101
	s_nop 0
	v_exp_f32_e32 v102, v102
	v_exp_f32_e32 v103, v103
	v_exp_f32_e32 v104, v104
	v_exp_f32_e32 v105, v105
	v_add_u32_e32 v52, s8, v232
	ds_read_b128 v[186:189], v52
	ds_read_b128 v[178:181], v52 offset:512
	v_exp_f32_e32 v106, v106
	v_exp_f32_e32 v107, v107
	v_exp_f32_e32 v108, v108
	v_exp_f32_e32 v109, v109
	ds_read_b128 v[182:185], v52 offset:2048
	ds_read_b128 v[170:173], v52 offset:2560
	v_exp_f32_e32 v110, v110
	v_exp_f32_e32 v111, v111
	v_exp_f32_e32 v112, v112
	v_exp_f32_e32 v113, v113
	ds_read_b128 v[174:177], v52 offset:4096
	ds_read_b128 v[154:157], v52 offset:4608
	v_exp_f32_e32 v82, v82
	v_exp_f32_e32 v83, v83
	v_exp_f32_e32 v84, v84
	v_exp_f32_e32 v85, v85
	ds_read_b128 v[162:165], v52 offset:6144
	ds_read_b128 v[146:149], v52 offset:6656
	v_exp_f32_e32 v86, v86
	v_exp_f32_e32 v87, v87
	v_exp_f32_e32 v88, v88
	v_exp_f32_e32 v89, v89
	s_nop 0
	v_exp_f32_e32 v90, v90
	v_exp_f32_e32 v91, v91
	v_exp_f32_e32 v92, v92
	v_exp_f32_e32 v93, v93
	s_nop 0
	v_exp_f32_e32 v94, v94
	v_exp_f32_e32 v95, v95
	v_exp_f32_e32 v96, v96
	v_exp_f32_e32 v97, v97
	s_waitcnt vmcnt(2) lgkmcnt(0)
	s_barrier
	s_add_i32 s42, s53, 0x2000
	v_mfma_f32_32x32x16_bf16 v[2:17], v[130:133], v[36:39], v[2:17]
	s_cmpk_lg_i32 s53, 0x4000
	v_add_f32_e32 v34, v34, v251
	s_cselect_b32 s52, s42, 0
	v_mfma_f32_32x32x16_bf16 v[18:33], v[130:133], v[40:43], v[18:33]
	v_mfma_f32_32x32x16_bf16 v[2:17], v[134:137], v[44:47], v[2:17]
	v_mfma_f32_32x32x16_bf16 v[18:33], v[134:137], v[66:69], v[18:33]
	v_mfma_f32_32x32x16_bf16 v[2:17], v[138:141], v[158:161], v[2:17]
	v_mfma_f32_32x32x16_bf16 v[18:33], v[138:141], v[48:51], v[18:33]
	v_mfma_f32_32x32x16_bf16 v[2:17], v[142:145], v[150:153], v[2:17]
	v_mfma_f32_32x32x16_bf16 v[18:33], v[142:145], v[166:169], v[18:33]
	v_mfma_f32_32x32x2_f32 v[66:81], v246, v244, 0
	v_mfma_f32_32x32x2_f32 v[50:65], v247, v244, 0
	s_mov_b32 exec_hi, 0
	ds_read_b32 v242, v245 offset:512
	ds_read_b32 v243, v245 offset:640
	s_mov_b32 exec_hi, -1
	v_add_u32_e32 v48, s41, v235
	ds_read_b64_tr_b16 v[36:37], v48 offset:24576
	ds_read_b64_tr_b16 v[38:39], v48 offset:25088
	v_mfma_f32_32x32x16_bf16 v[66:81], v[186:189], v[114:117], v[66:81]
	v_add_f32_e32 v40, v98, v99
	v_add_f32_e32 v40, v100, v40
	v_add_f32_e32 v40, v101, v40
	v_add_f32_e32 v40, v102, v40
	v_add_f32_e32 v44, v103, v40
	v_cvt_pk_bf16_f32 v130, v98, v99
	v_cvt_pk_bf16_f32 v131, v100, v101
	ds_read_b64_tr_b16 v[40:41], v48 offset:28672
	ds_read_b64_tr_b16 v[42:43], v48 offset:29184
	v_mfma_f32_32x32x16_bf16 v[50:65], v[178:181], v[114:117], v[50:65]
	v_add_f32_e32 v44, v104, v44
	v_add_f32_e32 v44, v105, v44
	v_add_f32_e32 v44, v106, v44
	v_add_f32_e32 v49, v107, v44
	v_cvt_pk_bf16_f32 v132, v102, v103
	v_cvt_pk_bf16_f32 v133, v104, v105
	ds_read_b64_tr_b16 v[44:45], v48 offset:25600
	ds_read_b64_tr_b16 v[46:47], v48 offset:26112
	v_mfma_f32_32x32x16_bf16 v[66:81], v[182:185], v[118:121], v[66:81]
	v_add_f32_e32 v49, v108, v49
	v_add_f32_e32 v49, v109, v49
	v_add_f32_e32 v49, v110, v49
	v_add_f32_e32 v49, v111, v49
	v_cvt_pk_bf16_f32 v134, v106, v107
	v_cvt_pk_bf16_f32 v135, v108, v109
	ds_read_b64_tr_b16 v[98:99], v48 offset:29696
	ds_read_b64_tr_b16 v[100:101], v48 offset:30208
	v_mfma_f32_32x32x16_bf16 v[50:65], v[170:173], v[118:121], v[50:65]
	v_add_f32_e32 v49, v112, v49
	v_add_f32_e32 v49, v113, v49
	v_add_f32_e32 v49, v82, v49
	v_add_f32_e32 v49, v83, v49
	v_cvt_pk_bf16_f32 v136, v110, v111
	v_cvt_pk_bf16_f32 v137, v112, v113
	ds_read_b64_tr_b16 v[102:103], v48 offset:26624
	ds_read_b64_tr_b16 v[104:105], v48 offset:27136
	v_mfma_f32_32x32x16_bf16 v[66:81], v[174:177], v[122:125], v[66:81]
	v_add_f32_e32 v49, v84, v49
	v_add_f32_e32 v49, v85, v49
	v_add_f32_e32 v49, v86, v49
	v_add_f32_e32 v49, v87, v49
	v_cvt_pk_bf16_f32 v138, v82, v83
	v_cvt_pk_bf16_f32 v139, v84, v85
	ds_read_b64_tr_b16 v[82:83], v48 offset:30720
	ds_read_b64_tr_b16 v[84:85], v48 offset:31232
	v_mfma_f32_32x32x16_bf16 v[50:65], v[154:157], v[122:125], v[50:65]
	v_add_f32_e32 v49, v88, v49
	v_add_f32_e32 v49, v89, v49
	v_add_f32_e32 v49, v90, v49
	v_add_f32_e32 v49, v91, v49
	v_cvt_pk_bf16_f32 v140, v86, v87
	v_cvt_pk_bf16_f32 v141, v88, v89
	ds_read_b64_tr_b16 v[86:87], v48 offset:27648
	ds_read_b64_tr_b16 v[88:89], v48 offset:28160
	v_mfma_f32_32x32x16_bf16 v[66:81], v[162:165], v[126:129], v[66:81]
	v_add_f32_e32 v49, v92, v49
	v_add_f32_e32 v49, v93, v49
	v_add_f32_e32 v49, v94, v49
	v_add_f32_e32 v49, v95, v49
	v_cvt_pk_bf16_f32 v142, v90, v91
	v_cvt_pk_bf16_f32 v143, v92, v93
	ds_read_b64_tr_b16 v[90:91], v48 offset:31744
	ds_read_b64_tr_b16 v[92:93], v48 offset:32256
	v_mfma_f32_32x32x16_bf16 v[50:65], v[146:149], v[126:129], v[50:65]
	v_add_f32_e32 v48, v96, v49
	v_add_f32_e32 v48, v97, v48
	v_add_f32_e32 v48, 0, v48
	v_cvt_pk_bf16_f32 v144, v94, v95
	v_cvt_pk_bf16_f32 v145, v96, v97
	s_add_i32 s41, s53, s50
	s_mov_b32 s42, m0
	s_mov_b32 m0, s41
	s_nop 0
	global_load_lds_dwordx4 v[220:221], off
	s_mov_b32 m0, s42
	s_add_i32 s41, s52, s51
	s_mov_b32 s42, m0
	s_mov_b32 m0, s41
	s_nop 0
	global_load_lds_dwordx4 v[218:219], off
	s_mov_b32 m0, s42
	v_add_f32_e32 v34, v34, v48
	s_add_i32 s30, s30, 2
	s_waitcnt lgkmcnt(14)
	v_mfma_f32_32x32x16_bf16 v[2:17], v[130:133], v[36:39], v[2:17]
	v_exp_f32_e32 v66, v66
	v_exp_f32_e32 v67, v67
	v_exp_f32_e32 v68, v68
	v_exp_f32_e32 v69, v69
	s_waitcnt lgkmcnt(12)
	v_mfma_f32_32x32x16_bf16 v[18:33], v[130:133], v[40:43], v[18:33]
	v_exp_f32_e32 v70, v70
	v_exp_f32_e32 v71, v71
	v_exp_f32_e32 v72, v72
	v_exp_f32_e32 v73, v73
	v_add_u32_e32 v36, s52, v232
	ds_read_b128 v[174:177], v36
	ds_read_b128 v[166:169], v36 offset:512
	s_waitcnt lgkmcnt(12)
	v_mfma_f32_32x32x16_bf16 v[2:17], v[134:137], v[44:47], v[2:17]
	v_exp_f32_e32 v74, v74
	v_exp_f32_e32 v75, v75
	v_exp_f32_e32 v76, v76
	v_exp_f32_e32 v77, v77
	ds_read_b128 v[170:173], v36 offset:2048
	ds_read_b128 v[158:161], v36 offset:2560
	s_waitcnt lgkmcnt(12)
	v_mfma_f32_32x32x16_bf16 v[18:33], v[134:137], v[98:101], v[18:33]
	v_exp_f32_e32 v78, v78
	v_exp_f32_e32 v79, v79
	v_exp_f32_e32 v80, v80
	v_exp_f32_e32 v81, v81
	ds_read_b128 v[162:165], v36 offset:4096
	ds_read_b128 v[150:153], v36 offset:4608
	s_waitcnt lgkmcnt(12)
	v_mfma_f32_32x32x16_bf16 v[2:17], v[138:141], v[102:105], v[2:17]
	v_exp_f32_e32 v50, v50
	v_exp_f32_e32 v51, v51
	v_exp_f32_e32 v52, v52
	v_exp_f32_e32 v53, v53
	ds_read_b128 v[154:157], v36 offset:6144
	ds_read_b128 v[146:149], v36 offset:6656
	s_waitcnt lgkmcnt(12)
	v_mfma_f32_32x32x16_bf16 v[18:33], v[138:141], v[82:85], v[18:33]
	v_exp_f32_e32 v54, v54
	v_exp_f32_e32 v55, v55
	v_exp_f32_e32 v56, v56
	v_exp_f32_e32 v57, v57
	s_waitcnt lgkmcnt(10)
	v_mfma_f32_32x32x16_bf16 v[2:17], v[142:145], v[86:89], v[2:17]
	v_exp_f32_e32 v58, v58
	v_exp_f32_e32 v59, v59
	v_exp_f32_e32 v60, v60
	v_exp_f32_e32 v61, v61
	s_waitcnt lgkmcnt(8)
	v_mfma_f32_32x32x16_bf16 v[18:33], v[142:145], v[90:93], v[18:33]
	v_exp_f32_e32 v62, v62
	v_exp_f32_e32 v63, v63
	v_exp_f32_e32 v64, v64
	v_exp_f32_e32 v65, v65
	s_waitcnt vmcnt(2) lgkmcnt(0)
	s_barrier
	s_add_i32 s41, s52, 0x2000
	s_cmpk_lg_i32 s52, 0x4000
	s_cselect_b32 s53, s41, 0
	v_lshl_add_u64 v[218:219], v[218:219], 0, s[14:15]
	v_lshl_add_u64 v[220:221], v[220:221], 0, s[14:15]
	v_add_u32_e32 v35, 0x200, v35
	v_add_u32_e32 v245, 0x200, v245
	s_cmp_ge_i32 s30, s9
	s_mov_b32 s42, s8
	s_cbranch_scc0 .LBB0_1702
	s_add_i32 s9, s30, 1
	s_cmp_ge_i32 s9, s49
	s_cbranch_scc1 .LBB0_1742
